# v27 + P8 epilogue: adjacent squares packed into v_pk_mul_f32 (57 fewer VALU per lane per tile)
# baseline (speedup 1.0000x reference)
; __device__ __forceinline__ unsigned pk4_fp8(float a, float b, float c, float d) {
;     a = fminf(fmaxf(a, -448.f), 448.f); b = fminf(fmaxf(b, -448.f), 448.f); c = fminf(fmaxf(c, -448.f), 448.f); d = fminf(fmaxf(d, -448.f), 448.f);
;     int w = 0; w = __builtin_amdgcn_cvt_pk_fp8_f32(a, b, w, false); w = __builtin_amdgcn_cvt_pk_fp8_f32(c, d, w, true); return (unsigned)w;
;     __device__ __forceinline__ void operator()(const f32x4 (&acc)[2][2][4][2], const Unit& u, int wr, int wc, int fr, int fq) const {
;     ...
;                 const int row = row0 + ai * HALF + m * 16;
;                 const float rs = rsqrtf(ss[row] * (1.0f / 4096.0f) + RMS_EPS) * (1.0f / 64.0f);
;                 unsigned char* rowp = U + ((size_t)(row >> 4) * 512 + (col0 >> 5)) * 512 + (row & 15) * 32 + (col0 & 31);
; #pragma unroll
;                 for (int bj = 0; bj < 2; ++bj) {
;                     f32x4 v0 = acc[ai][bj][m][0] * rs, v1 = acc[ai][bj][m][1] * rs;
; #pragma unroll
;                     for (int j = 0; j < 4; ++j) { const float a = fmaxf(v0[j], 0.f), b = fmaxf(v1[j], 0.f); v0[j] = a * a * 4.f; v1[j] = b * b * 4.f; }
;                     u32x2 w; w.x = pk4_fp8(v0[0], v0[1], v0[2], v0[3]); w.y = pk4_fp8(v1[0], v1[1], v1[2], v1[3]);
;                     *(u32x2*)(rowp + bj * (HALF / 32) * 512) = w;
.LBB0_2284:
	s_lshl_b32 s13, s20, 8
	s_add_i32 s13, s13, s36
	v_or_b32_e32 v2, s13, v1
	v_ashrrev_i32_e32 v3, 31, v2
	s_nop 15
	s_nop 15
	v_lshl_add_u64 v[4:5], v[2:3], 2, s[2:3]
	s_lshl_b32 s15, s21, 8
	s_or_b32 s15, s15, s37
	v_mov_b32_e32 v6, 0
	v_mov_b32_e32 v7, 0
	s_ashr_i32 s20, s15, 5
	s_ashr_i32 s22, s13, 4
	v_mov_b32_e32 v8, 0
	s_ashr_i32 s21, s20, 31
	s_ashr_i32 s23, s22, 31
	s_lshl_b64 s[20:21], s[20:21], 9
	s_lshl_b64 s[22:23], s[22:23], 18
	v_readlane_b32 s24, v253, 46
	v_readlane_b32 s25, v253, 47
	s_add_u32 s13, s24, s22
	s_addc_u32 s15, s25, s23
	s_add_u32 s22, s13, s20
	s_addc_u32 s23, s15, s21
	s_waitcnt vmcnt(0)
	v_fmamk_f32 v3, v234, 0x39800000, v194
	v_mul_f32_e32 v9, 0x4b800000, v3
	v_cmp_gt_f32_e32 vcc, s43, v3
	s_nop 1
	v_cndmask_b32_e32 v3, v3, v9, vcc
	v_rsq_f32_e32 v3, v3
	s_nop 0
	v_mul_f32_e32 v9, 0x45800000, v3
	v_cndmask_b32_e32 v3, v3, v9, vcc
	v_mul_f32_e32 v10, 0x3d000000, v3
	v_pk_mul_f32 v[14:15], v[158:159], v[10:11] op_sel_hi:[1,0]
	v_pk_mul_f32 v[18:19], v[154:155], v[10:11] op_sel_hi:[1,0]
	v_pk_mul_f32 v[12:13], v[160:161], v[10:11] op_sel_hi:[1,0]
	v_pk_mul_f32 v[16:17], v[156:157], v[10:11] op_sel_hi:[1,0]
	v_pk_mul_f32 v[20:21], v[152:153], v[10:11] op_sel_hi:[1,0]
	v_pk_mul_f32 v[22:23], v[150:151], v[10:11] op_sel_hi:[1,0]
	v_pk_mul_f32 v[24:25], v[148:149], v[10:11] op_sel_hi:[1,0]
	v_pk_mul_f32 v[10:11], v[146:147], v[10:11] op_sel_hi:[1,0]
	v_max_f32_e32 v3, 0, v14
	v_max_f32_e32 v9, 0, v18
	v_max_f32_e32 v14, 0, v15
	v_max_f32_e32 v15, 0, v19
	v_max_f32_e32 v18, 0, v22
	v_max_f32_e32 v10, 0, v10
	v_max_f32_e32 v19, 0, v23
	v_max_f32_e32 v11, 0, v11
	v_mul_f32_e32 v3, v3, v3
	v_mul_f32_e32 v9, v9, v9
	v_pk_mul_f32 v[14:15], v[14:15], v[14:15]
	v_pk_mul_f32 v[18:19], v[18:19], v[18:19]
	v_pk_mul_f32 v[10:11], v[10:11], v[10:11]
	v_med3_f32 v3, v3, s44, v195
	v_med3_f32 v14, v14, s44, v195
	v_med3_f32 v9, v9, s44, v195
	v_med3_f32 v15, v15, s44, v195
	v_max_f32_e32 v12, 0, v12
	v_max_f32_e32 v16, 0, v16
	v_max_f32_e32 v13, 0, v13
	v_max_f32_e32 v17, 0, v17
	v_med3_f32 v18, v18, s44, v195
	v_med3_f32 v19, v19, s44, v195
	v_med3_f32 v10, v10, s44, v195
	v_cvt_pk_fp8_f32 v6, v3, v14
	v_cvt_pk_fp8_f32 v7, v9, v15
	v_med3_f32 v3, v11, s44, v195
	v_mov_b32_e32 v9, 0
	v_max_f32_e32 v20, 0, v20
	v_max_f32_e32 v22, 0, v24
	v_max_f32_e32 v21, 0, v21
	v_max_f32_e32 v23, 0, v25
	v_pk_mul_f32 v[12:13], v[12:13], v[12:13]
	v_pk_mul_f32 v[16:17], v[16:17], v[16:17]
	v_cvt_pk_fp8_f32 v8, v18, v19
	v_cvt_pk_fp8_f32 v9, v10, v3
	v_pk_mul_f32 v[20:21], v[20:21], v[20:21]
	v_pk_mul_f32 v[22:23], v[22:23], v[22:23]
	v_med3_f32 v12, v12, s44, v195
	v_med3_f32 v13, v13, s44, v195
	v_med3_f32 v16, v16, s44, v195
	v_med3_f32 v17, v17, s44, v195
	v_med3_f32 v20, v20, s44, v195
	v_med3_f32 v21, v21, s44, v195
	v_cvt_pk_fp8_f32 v6, v12, v13 op_sel:[0,0,1]
	v_cvt_pk_fp8_f32 v7, v16, v17 op_sel:[0,0,1]
	v_med3_f32 v3, v22, s44, v195
	v_med3_f32 v10, v23, s44, v195
	v_cvt_pk_fp8_f32 v8, v20, v21 op_sel:[0,0,1]
	v_cvt_pk_fp8_f32 v9, v3, v10 op_sel:[0,0,1]
	v_lshl_add_u64 v[10:11], s[22:23], 0, v[172:173]
	v_lshl_add_u64 v[10:11], v[10:11], 0, v[170:171]
	global_store_dwordx2 v[10:11], v[6:7], off
	global_store_dwordx2 v[10:11], v[8:9], off offset:2048
	v_or_b32_e32 v6, 16, v2
	v_ashrrev_i32_e32 v7, 31, v6
	v_lshl_add_u64 v[8:9], v[6:7], 2, s[2:3]
	v_mov_b32_e32 v8, 0
	v_mov_b32_e32 v9, 0
	v_mov_b32_e32 v10, 0
	v_ashrrev_i32_e32 v6, 4, v6
	v_ashrrev_i32_e32 v7, 31, v6
	v_lshlrev_b64 v[6:7], 18, v[6:7]
	v_lshl_add_u64 v[6:7], s[24:25], 0, v[6:7]
	v_lshl_add_u64 v[6:7], v[6:7], 0, s[20:21]
	v_lshl_add_u64 v[6:7], v[6:7], 0, v[172:173]
	v_lshl_add_u64 v[6:7], v[6:7], 0, v[170:171]
	v_fmamk_f32 v3, v235, 0x39800000, v194
	v_mul_f32_e32 v11, 0x4b800000, v3
	v_cmp_gt_f32_e32 vcc, s43, v3
	s_nop 1
	v_cndmask_b32_e32 v3, v3, v11, vcc
	v_rsq_f32_e32 v3, v3
	s_nop 0
	v_mul_f32_e32 v11, 0x45800000, v3
	v_cndmask_b32_e32 v3, v3, v11, vcc
	v_mul_f32_e32 v12, 0x3d000000, v3
	v_pk_mul_f32 v[16:17], v[142:143], v[12:13] op_sel_hi:[1,0]
	v_pk_mul_f32 v[20:21], v[138:139], v[12:13] op_sel_hi:[1,0]
	v_pk_mul_f32 v[14:15], v[144:145], v[12:13] op_sel_hi:[1,0]
	v_pk_mul_f32 v[18:19], v[140:141], v[12:13] op_sel_hi:[1,0]
	v_pk_mul_f32 v[22:23], v[136:137], v[12:13] op_sel_hi:[1,0]
	v_pk_mul_f32 v[24:25], v[134:135], v[12:13] op_sel_hi:[1,0]
	v_pk_mul_f32 v[26:27], v[132:133], v[12:13] op_sel_hi:[1,0]
	v_pk_mul_f32 v[12:13], v[130:131], v[12:13] op_sel_hi:[1,0]
	v_max_f32_e32 v3, 0, v16
	v_max_f32_e32 v11, 0, v20
	v_max_f32_e32 v16, 0, v17
	v_max_f32_e32 v17, 0, v21
	v_max_f32_e32 v20, 0, v24
	v_max_f32_e32 v12, 0, v12
	v_max_f32_e32 v21, 0, v25
	v_max_f32_e32 v13, 0, v13
	v_mul_f32_e32 v3, v3, v3
	v_mul_f32_e32 v11, v11, v11
	v_pk_mul_f32 v[16:17], v[16:17], v[16:17]
	v_pk_mul_f32 v[20:21], v[20:21], v[20:21]
	v_pk_mul_f32 v[12:13], v[12:13], v[12:13]
	v_med3_f32 v3, v3, s44, v195
	v_med3_f32 v16, v16, s44, v195
	v_med3_f32 v11, v11, s44, v195
	v_med3_f32 v17, v17, s44, v195
	v_max_f32_e32 v14, 0, v14
	v_max_f32_e32 v18, 0, v18
	v_max_f32_e32 v15, 0, v15
	v_max_f32_e32 v19, 0, v19
	v_med3_f32 v20, v20, s44, v195
	v_med3_f32 v21, v21, s44, v195
	v_cvt_pk_fp8_f32 v8, v3, v16
	v_cvt_pk_fp8_f32 v9, v11, v17
	v_med3_f32 v3, v12, s44, v195
	v_med3_f32 v12, v13, s44, v195
	v_mov_b32_e32 v11, 0
	v_max_f32_e32 v22, 0, v22
	v_max_f32_e32 v24, 0, v26
	v_max_f32_e32 v23, 0, v23
	v_max_f32_e32 v25, 0, v27
	v_pk_mul_f32 v[14:15], v[14:15], v[14:15]
	v_pk_mul_f32 v[18:19], v[18:19], v[18:19]
	v_cvt_pk_fp8_f32 v10, v20, v21
	v_cvt_pk_fp8_f32 v11, v3, v12
	v_pk_mul_f32 v[22:23], v[22:23], v[22:23]
	v_pk_mul_f32 v[24:25], v[24:25], v[24:25]
	v_med3_f32 v14, v14, s44, v195
; __device__ __forceinline__ unsigned pk4_fp8(float a, float b, float c, float d) {
;     a = fminf(fmaxf(a, -448.f), 448.f); b = fminf(fmaxf(b, -448.f), 448.f); c = fminf(fmaxf(c, -448.f), 448.f); d = fminf(fmaxf(d, -448.f), 448.f);
;     int w = 0; w = __builtin_amdgcn_cvt_pk_fp8_f32(a, b, w, false); w = __builtin_amdgcn_cvt_pk_fp8_f32(c, d, w, true); return (unsigned)w;
;     __device__ __forceinline__ void operator()(const f32x4 (&acc)[2][2][4][2], const Unit& u, int wr, int wc, int fr, int fq) const {
;     ...
;                 const int row = row0 + ai * HALF + m * 16;
;                 const float rs = rsqrtf(ss[row] * (1.0f / 4096.0f) + RMS_EPS) * (1.0f / 64.0f);
;                 unsigned char* rowp = U + ((size_t)(row >> 4) * 512 + (col0 >> 5)) * 512 + (row & 15) * 32 + (col0 & 31);
; #pragma unroll
;                 for (int bj = 0; bj < 2; ++bj) {
;                     f32x4 v0 = acc[ai][bj][m][0] * rs, v1 = acc[ai][bj][m][1] * rs;
; #pragma unroll
;                     for (int j = 0; j < 4; ++j) { const float a = fmaxf(v0[j], 0.f), b = fmaxf(v1[j], 0.f); v0[j] = a * a * 4.f; v1[j] = b * b * 4.f; }
;                     u32x2 w; w.x = pk4_fp8(v0[0], v0[1], v0[2], v0[3]); w.y = pk4_fp8(v1[0], v1[1], v1[2], v1[3]);
;                     *(u32x2*)(rowp + bj * (HALF / 32) * 512) = w;
	v_med3_f32 v15, v15, s44, v195
	v_med3_f32 v18, v18, s44, v195
	v_med3_f32 v19, v19, s44, v195
	v_med3_f32 v22, v22, s44, v195
	v_med3_f32 v23, v23, s44, v195
	v_cvt_pk_fp8_f32 v8, v14, v15 op_sel:[0,0,1]
	v_cvt_pk_fp8_f32 v9, v18, v19 op_sel:[0,0,1]
	v_med3_f32 v3, v24, s44, v195
	v_med3_f32 v12, v25, s44, v195
	v_cvt_pk_fp8_f32 v10, v22, v23 op_sel:[0,0,1]
	v_cvt_pk_fp8_f32 v11, v3, v12 op_sel:[0,0,1]
	global_store_dwordx2 v[6:7], v[8:9], off
	global_store_dwordx2 v[6:7], v[10:11], off offset:2048
	v_or_b32_e32 v6, 32, v2
	v_ashrrev_i32_e32 v7, 31, v6
	v_lshl_add_u64 v[8:9], v[6:7], 2, s[2:3]
	v_mov_b32_e32 v8, 0
	v_mov_b32_e32 v9, 0
	v_mov_b32_e32 v10, 0
	v_ashrrev_i32_e32 v6, 4, v6
	v_ashrrev_i32_e32 v7, 31, v6
	v_lshlrev_b64 v[6:7], 18, v[6:7]
	v_lshl_add_u64 v[6:7], s[24:25], 0, v[6:7]
	v_lshl_add_u64 v[6:7], v[6:7], 0, s[20:21]
	v_lshl_add_u64 v[6:7], v[6:7], 0, v[172:173]
	v_lshl_add_u64 v[6:7], v[6:7], 0, v[170:171]
	v_fmamk_f32 v3, v236, 0x39800000, v194
	v_mul_f32_e32 v11, 0x4b800000, v3
	v_cmp_gt_f32_e32 vcc, s43, v3
	s_nop 1
	v_cndmask_b32_e32 v3, v3, v11, vcc
	v_rsq_f32_e32 v3, v3
	s_nop 0
	v_mul_f32_e32 v11, 0x45800000, v3
	v_cndmask_b32_e32 v3, v3, v11, vcc
	v_mul_f32_e32 v12, 0x3d000000, v3
	v_pk_mul_f32 v[16:17], v[126:127], v[12:13] op_sel_hi:[1,0]
	v_pk_mul_f32 v[20:21], v[122:123], v[12:13] op_sel_hi:[1,0]
	v_pk_mul_f32 v[24:25], v[118:119], v[12:13] op_sel_hi:[1,0]
	v_pk_mul_f32 v[14:15], v[128:129], v[12:13] op_sel_hi:[1,0]
	v_pk_mul_f32 v[18:19], v[124:125], v[12:13] op_sel_hi:[1,0]
	v_pk_mul_f32 v[22:23], v[120:121], v[12:13] op_sel_hi:[1,0]
	v_pk_mul_f32 v[26:27], v[116:117], v[12:13] op_sel_hi:[1,0]
	v_pk_mul_f32 v[12:13], v[114:115], v[12:13] op_sel_hi:[1,0]
	v_max_f32_e32 v3, 0, v16
	v_max_f32_e32 v11, 0, v20
	v_max_f32_e32 v16, 0, v17
	v_max_f32_e32 v17, 0, v21
	v_max_f32_e32 v20, 0, v24
	v_max_f32_e32 v21, 0, v25
	v_max_f32_e32 v12, 0, v12
	v_max_f32_e32 v13, 0, v13
	v_mul_f32_e32 v3, v3, v3
	v_mul_f32_e32 v11, v11, v11
	v_pk_mul_f32 v[16:17], v[16:17], v[16:17]
	v_pk_mul_f32 v[20:21], v[20:21], v[20:21]
	v_pk_mul_f32 v[12:13], v[12:13], v[12:13]
	v_med3_f32 v3, v3, s44, v195
	v_med3_f32 v16, v16, s44, v195
	v_med3_f32 v11, v11, s44, v195
	v_med3_f32 v17, v17, s44, v195
	v_med3_f32 v20, v20, s44, v195
	v_med3_f32 v21, v21, s44, v195
	v_max_f32_e32 v14, 0, v14
	v_max_f32_e32 v18, 0, v18
	v_max_f32_e32 v15, 0, v15
	v_max_f32_e32 v19, 0, v19
	v_max_f32_e32 v22, 0, v22
	v_max_f32_e32 v23, 0, v23
	v_cvt_pk_fp8_f32 v8, v3, v16
	v_cvt_pk_fp8_f32 v9, v11, v17
	v_cvt_pk_fp8_f32 v10, v20, v21
	v_med3_f32 v12, v12, s44, v195
	v_med3_f32 v13, v13, s44, v195
	v_mov_b32_e32 v11, 0
	v_max_f32_e32 v24, 0, v26
	v_max_f32_e32 v25, 0, v27
	v_pk_mul_f32 v[14:15], v[14:15], v[14:15]
	v_pk_mul_f32 v[18:19], v[18:19], v[18:19]
	v_pk_mul_f32 v[22:23], v[22:23], v[22:23]
	v_cvt_pk_fp8_f32 v11, v12, v13
	v_pk_mul_f32 v[24:25], v[24:25], v[24:25]
	v_med3_f32 v14, v14, s44, v195
	v_med3_f32 v15, v15, s44, v195
	v_med3_f32 v18, v18, s44, v195
	v_med3_f32 v19, v19, s44, v195
	v_med3_f32 v22, v22, s44, v195
	v_med3_f32 v3, v23, s44, v195
	v_cvt_pk_fp8_f32 v8, v14, v15 op_sel:[0,0,1]
	v_cvt_pk_fp8_f32 v9, v18, v19 op_sel:[0,0,1]
	v_cvt_pk_fp8_f32 v10, v22, v3 op_sel:[0,0,1]
	v_med3_f32 v3, v24, s44, v195
	v_med3_f32 v12, v25, s44, v195
	v_cvt_pk_fp8_f32 v11, v3, v12 op_sel:[0,0,1]
	global_store_dwordx2 v[6:7], v[8:9], off
	global_store_dwordx2 v[6:7], v[10:11], off offset:2048
	v_or_b32_e32 v6, 48, v2
	v_ashrrev_i32_e32 v7, 31, v6
	v_lshl_add_u64 v[8:9], v[6:7], 2, s[2:3]
	v_mov_b32_e32 v8, 0
	v_mov_b32_e32 v9, 0
	v_mov_b32_e32 v10, 0
	v_ashrrev_i32_e32 v6, 4, v6
	v_ashrrev_i32_e32 v7, 31, v6
	v_lshlrev_b64 v[6:7], 18, v[6:7]
	v_lshl_add_u64 v[6:7], s[24:25], 0, v[6:7]
	v_lshl_add_u64 v[6:7], v[6:7], 0, s[20:21]
	v_lshl_add_u64 v[6:7], v[6:7], 0, v[172:173]
	v_lshl_add_u64 v[6:7], v[6:7], 0, v[170:171]
	v_fmamk_f32 v3, v237, 0x39800000, v194
	v_mul_f32_e32 v11, 0x4b800000, v3
	v_cmp_gt_f32_e32 vcc, s43, v3
	s_nop 1
	v_cndmask_b32_e32 v3, v3, v11, vcc
	v_rsq_f32_e32 v3, v3
	s_nop 0
	v_mul_f32_e32 v11, 0x45800000, v3
	v_cndmask_b32_e32 v3, v3, v11, vcc
	v_mul_f32_e32 v12, 0x3d000000, v3
	v_pk_mul_f32 v[16:17], v[110:111], v[12:13] op_sel_hi:[1,0]
	v_pk_mul_f32 v[20:21], v[106:107], v[12:13] op_sel_hi:[1,0]
	v_pk_mul_f32 v[24:25], v[102:103], v[12:13] op_sel_hi:[1,0]
	v_pk_mul_f32 v[14:15], v[112:113], v[12:13] op_sel_hi:[1,0]
	v_pk_mul_f32 v[18:19], v[108:109], v[12:13] op_sel_hi:[1,0]
	v_pk_mul_f32 v[22:23], v[104:105], v[12:13] op_sel_hi:[1,0]
	v_pk_mul_f32 v[26:27], v[100:101], v[12:13] op_sel_hi:[1,0]
	v_pk_mul_f32 v[12:13], v[98:99], v[12:13] op_sel_hi:[1,0]
	v_max_f32_e32 v3, 0, v16
	v_max_f32_e32 v11, 0, v20
	v_max_f32_e32 v16, 0, v17
	v_max_f32_e32 v17, 0, v21
	v_max_f32_e32 v20, 0, v24
	v_max_f32_e32 v21, 0, v25
	v_max_f32_e32 v12, 0, v12
	v_max_f32_e32 v13, 0, v13
	v_mul_f32_e32 v3, v3, v3
	v_mul_f32_e32 v11, v11, v11
	v_pk_mul_f32 v[16:17], v[16:17], v[16:17]
	v_pk_mul_f32 v[20:21], v[20:21], v[20:21]
	v_pk_mul_f32 v[12:13], v[12:13], v[12:13]
	v_med3_f32 v3, v3, s44, v195
	v_med3_f32 v16, v16, s44, v195
	v_med3_f32 v11, v11, s44, v195
	v_med3_f32 v17, v17, s44, v195
	v_med3_f32 v20, v20, s44, v195
	v_med3_f32 v21, v21, s44, v195
	v_max_f32_e32 v14, 0, v14
	v_max_f32_e32 v18, 0, v18
	v_max_f32_e32 v15, 0, v15
	v_max_f32_e32 v19, 0, v19
	v_max_f32_e32 v22, 0, v22
	v_max_f32_e32 v23, 0, v23
	v_cvt_pk_fp8_f32 v8, v3, v16
	v_cvt_pk_fp8_f32 v9, v11, v17
	v_cvt_pk_fp8_f32 v10, v20, v21
	v_med3_f32 v12, v12, s44, v195
	v_med3_f32 v13, v13, s44, v195
	v_mov_b32_e32 v11, 0
	v_max_f32_e32 v24, 0, v26
	v_max_f32_e32 v25, 0, v27
; __device__ __forceinline__ unsigned pk4_fp8(float a, float b, float c, float d) {
;     a = fminf(fmaxf(a, -448.f), 448.f); b = fminf(fmaxf(b, -448.f), 448.f); c = fminf(fmaxf(c, -448.f), 448.f); d = fminf(fmaxf(d, -448.f), 448.f);
;     int w = 0; w = __builtin_amdgcn_cvt_pk_fp8_f32(a, b, w, false); w = __builtin_amdgcn_cvt_pk_fp8_f32(c, d, w, true); return (unsigned)w;
;     __device__ __forceinline__ void operator()(const f32x4 (&acc)[2][2][4][2], const Unit& u, int wr, int wc, int fr, int fq) const {
;     ...
;                 const int row = row0 + ai * HALF + m * 16;
;                 const float rs = rsqrtf(ss[row] * (1.0f / 4096.0f) + RMS_EPS) * (1.0f / 64.0f);
;                 unsigned char* rowp = U + ((size_t)(row >> 4) * 512 + (col0 >> 5)) * 512 + (row & 15) * 32 + (col0 & 31);
; #pragma unroll
;                 for (int bj = 0; bj < 2; ++bj) {
;                     f32x4 v0 = acc[ai][bj][m][0] * rs, v1 = acc[ai][bj][m][1] * rs;
; #pragma unroll
;                     for (int j = 0; j < 4; ++j) { const float a = fmaxf(v0[j], 0.f), b = fmaxf(v1[j], 0.f); v0[j] = a * a * 4.f; v1[j] = b * b * 4.f; }
;                     u32x2 w; w.x = pk4_fp8(v0[0], v0[1], v0[2], v0[3]); w.y = pk4_fp8(v1[0], v1[1], v1[2], v1[3]);
;                     *(u32x2*)(rowp + bj * (HALF / 32) * 512) = w;
	v_pk_mul_f32 v[14:15], v[14:15], v[14:15]
	v_pk_mul_f32 v[18:19], v[18:19], v[18:19]
	v_pk_mul_f32 v[22:23], v[22:23], v[22:23]
	v_cvt_pk_fp8_f32 v11, v12, v13
	v_pk_mul_f32 v[24:25], v[24:25], v[24:25]
	v_med3_f32 v14, v14, s44, v195
	v_med3_f32 v15, v15, s44, v195
	v_med3_f32 v18, v18, s44, v195
	v_med3_f32 v19, v19, s44, v195
	v_med3_f32 v3, v22, s44, v195
	v_med3_f32 v16, v23, s44, v195
	v_cvt_pk_fp8_f32 v8, v14, v15 op_sel:[0,0,1]
	v_cvt_pk_fp8_f32 v9, v18, v19 op_sel:[0,0,1]
	v_cvt_pk_fp8_f32 v10, v3, v16 op_sel:[0,0,1]
	v_med3_f32 v3, v24, s44, v195
	v_med3_f32 v12, v25, s44, v195
	v_cvt_pk_fp8_f32 v11, v3, v12 op_sel:[0,0,1]
	global_store_dwordx2 v[6:7], v[8:9], off
	global_store_dwordx2 v[6:7], v[10:11], off offset:2048
	v_add_u32_e32 v9, 0x80, v2
	v_ashrrev_i32_e32 v10, 4, v9
	v_mov_b32_e32 v6, 0
	v_mov_b32_e32 v7, 0
	v_mov_b32_e32 v8, 0
	v_ashrrev_i32_e32 v11, 31, v10
	v_lshlrev_b64 v[10:11], 18, v[10:11]
	v_lshl_add_u64 v[10:11], s[24:25], 0, v[10:11]
	v_lshl_add_u64 v[10:11], v[10:11], 0, s[20:21]
	v_lshl_add_u64 v[10:11], v[10:11], 0, v[172:173]
	v_lshl_add_u64 v[10:11], v[10:11], 0, v[170:171]
	v_fmamk_f32 v3, v238, 0x39800000, v194
	v_mul_f32_e32 v9, 0x4b800000, v3
	v_cmp_gt_f32_e32 vcc, s43, v3
	s_nop 1
	v_cndmask_b32_e32 v3, v3, v9, vcc
	v_rsq_f32_e32 v3, v3
	s_nop 0
	v_mul_f32_e32 v9, 0x45800000, v3
	v_cndmask_b32_e32 v3, v3, v9, vcc
	v_mul_f32_e32 v12, 0x3d000000, v3
	v_pk_mul_f32 v[16:17], v[94:95], v[12:13] op_sel_hi:[1,0]
	v_pk_mul_f32 v[20:21], v[90:91], v[12:13] op_sel_hi:[1,0]
	v_pk_mul_f32 v[24:25], v[86:87], v[12:13] op_sel_hi:[1,0]
	v_pk_mul_f32 v[14:15], v[96:97], v[12:13] op_sel_hi:[1,0]
	v_pk_mul_f32 v[18:19], v[92:93], v[12:13] op_sel_hi:[1,0]
	v_pk_mul_f32 v[22:23], v[88:89], v[12:13] op_sel_hi:[1,0]
	v_pk_mul_f32 v[26:27], v[84:85], v[12:13] op_sel_hi:[1,0]
	v_pk_mul_f32 v[12:13], v[82:83], v[12:13] op_sel_hi:[1,0]
	v_max_f32_e32 v3, 0, v16
	v_max_f32_e32 v9, 0, v20
	v_max_f32_e32 v16, 0, v17
	v_max_f32_e32 v17, 0, v21
	v_max_f32_e32 v20, 0, v24
	v_max_f32_e32 v21, 0, v25
	v_max_f32_e32 v12, 0, v12
	v_max_f32_e32 v13, 0, v13
	v_mul_f32_e32 v3, v3, v3
	v_mul_f32_e32 v9, v9, v9
	v_pk_mul_f32 v[16:17], v[16:17], v[16:17]
	v_pk_mul_f32 v[20:21], v[20:21], v[20:21]
	v_pk_mul_f32 v[12:13], v[12:13], v[12:13]
	v_med3_f32 v3, v3, s44, v195
	v_med3_f32 v16, v16, s44, v195
	v_med3_f32 v9, v9, s44, v195
	v_med3_f32 v17, v17, s44, v195
	v_med3_f32 v20, v20, s44, v195
	v_med3_f32 v21, v21, s44, v195
	v_max_f32_e32 v14, 0, v14
	v_max_f32_e32 v18, 0, v18
	v_max_f32_e32 v15, 0, v15
	v_max_f32_e32 v19, 0, v19
	v_max_f32_e32 v22, 0, v22
	v_max_f32_e32 v23, 0, v23
	v_cvt_pk_fp8_f32 v6, v3, v16
	v_cvt_pk_fp8_f32 v7, v9, v17
	v_cvt_pk_fp8_f32 v8, v20, v21
	v_med3_f32 v12, v12, s44, v195
	v_med3_f32 v13, v13, s44, v195
	v_mov_b32_e32 v9, 0
	v_max_f32_e32 v24, 0, v26
	v_max_f32_e32 v25, 0, v27
	v_pk_mul_f32 v[14:15], v[14:15], v[14:15]
	v_pk_mul_f32 v[18:19], v[18:19], v[18:19]
	v_pk_mul_f32 v[22:23], v[22:23], v[22:23]
	v_cvt_pk_fp8_f32 v9, v12, v13
	v_pk_mul_f32 v[24:25], v[24:25], v[24:25]
	v_med3_f32 v14, v14, s44, v195
	v_med3_f32 v15, v15, s44, v195
	v_med3_f32 v18, v18, s44, v195
	v_med3_f32 v19, v19, s44, v195
	v_med3_f32 v22, v22, s44, v195
	v_med3_f32 v3, v23, s44, v195
	v_cvt_pk_fp8_f32 v6, v14, v15 op_sel:[0,0,1]
	v_cvt_pk_fp8_f32 v7, v18, v19 op_sel:[0,0,1]
	v_cvt_pk_fp8_f32 v8, v22, v3 op_sel:[0,0,1]
	v_med3_f32 v3, v24, s44, v195
	v_med3_f32 v12, v25, s44, v195
	v_cvt_pk_fp8_f32 v9, v3, v12 op_sel:[0,0,1]
	global_store_dwordx2 v[10:11], v[6:7], off
	global_store_dwordx2 v[10:11], v[8:9], off offset:2048
	v_add_u32_e32 v9, 0x90, v2
	v_ashrrev_i32_e32 v10, 4, v9
	v_mov_b32_e32 v6, 0
	v_mov_b32_e32 v7, 0
	v_mov_b32_e32 v8, 0
	v_ashrrev_i32_e32 v11, 31, v10
	v_lshlrev_b64 v[10:11], 18, v[10:11]
	v_lshl_add_u64 v[10:11], s[24:25], 0, v[10:11]
	v_lshl_add_u64 v[10:11], v[10:11], 0, s[20:21]
	v_lshl_add_u64 v[10:11], v[10:11], 0, v[172:173]
	v_lshl_add_u64 v[10:11], v[10:11], 0, v[170:171]
	v_fmamk_f32 v3, v239, 0x39800000, v194
	v_mul_f32_e32 v9, 0x4b800000, v3
	v_cmp_gt_f32_e32 vcc, s43, v3
	s_nop 1
	v_cndmask_b32_e32 v3, v3, v9, vcc
	v_rsq_f32_e32 v3, v3
	s_nop 0
	v_mul_f32_e32 v9, 0x45800000, v3
	v_cndmask_b32_e32 v3, v3, v9, vcc
	v_mul_f32_e32 v12, 0x3d000000, v3
	v_pk_mul_f32 v[16:17], v[78:79], v[12:13] op_sel_hi:[1,0]
	v_pk_mul_f32 v[20:21], v[74:75], v[12:13] op_sel_hi:[1,0]
	v_pk_mul_f32 v[14:15], v[80:81], v[12:13] op_sel_hi:[1,0]
	v_pk_mul_f32 v[18:19], v[76:77], v[12:13] op_sel_hi:[1,0]
	v_pk_mul_f32 v[22:23], v[72:73], v[12:13] op_sel_hi:[1,0]
	v_pk_mul_f32 v[24:25], v[70:71], v[12:13] op_sel_hi:[1,0]
	v_pk_mul_f32 v[26:27], v[68:69], v[12:13] op_sel_hi:[1,0]
	v_pk_mul_f32 v[12:13], v[66:67], v[12:13] op_sel_hi:[1,0]
	v_max_f32_e32 v3, 0, v16
	v_max_f32_e32 v9, 0, v20
	v_max_f32_e32 v16, 0, v17
	v_max_f32_e32 v17, 0, v21
	v_max_f32_e32 v20, 0, v24
	v_max_f32_e32 v12, 0, v12
	v_max_f32_e32 v21, 0, v25
	v_max_f32_e32 v13, 0, v13
	v_mul_f32_e32 v3, v3, v3
	v_mul_f32_e32 v9, v9, v9
	v_pk_mul_f32 v[16:17], v[16:17], v[16:17]
	v_pk_mul_f32 v[20:21], v[20:21], v[20:21]
	v_pk_mul_f32 v[12:13], v[12:13], v[12:13]
	v_med3_f32 v3, v3, s44, v195
	v_med3_f32 v16, v16, s44, v195
	v_med3_f32 v9, v9, s44, v195
	v_med3_f32 v17, v17, s44, v195
	v_max_f32_e32 v14, 0, v14
	v_max_f32_e32 v18, 0, v18
	v_max_f32_e32 v15, 0, v15
	v_max_f32_e32 v19, 0, v19
	v_med3_f32 v20, v20, s44, v195
	v_med3_f32 v21, v21, s44, v195
	v_cvt_pk_fp8_f32 v6, v3, v16
	v_cvt_pk_fp8_f32 v7, v9, v17
	v_med3_f32 v3, v12, s44, v195
	v_med3_f32 v12, v13, s44, v195
	v_mov_b32_e32 v9, 0
	v_max_f32_e32 v22, 0, v22
	v_max_f32_e32 v24, 0, v26
; __device__ __forceinline__ unsigned pk4_fp8(float a, float b, float c, float d) {
;     a = fminf(fmaxf(a, -448.f), 448.f); b = fminf(fmaxf(b, -448.f), 448.f); c = fminf(fmaxf(c, -448.f), 448.f); d = fminf(fmaxf(d, -448.f), 448.f);
;     int w = 0; w = __builtin_amdgcn_cvt_pk_fp8_f32(a, b, w, false); w = __builtin_amdgcn_cvt_pk_fp8_f32(c, d, w, true); return (unsigned)w;
;     __device__ __forceinline__ void operator()(const f32x4 (&acc)[2][2][4][2], const Unit& u, int wr, int wc, int fr, int fq) const {
;     ...
;                 const int row = row0 + ai * HALF + m * 16;
;                 const float rs = rsqrtf(ss[row] * (1.0f / 4096.0f) + RMS_EPS) * (1.0f / 64.0f);
;                 unsigned char* rowp = U + ((size_t)(row >> 4) * 512 + (col0 >> 5)) * 512 + (row & 15) * 32 + (col0 & 31);
; #pragma unroll
;                 for (int bj = 0; bj < 2; ++bj) {
;                     f32x4 v0 = acc[ai][bj][m][0] * rs, v1 = acc[ai][bj][m][1] * rs;
; #pragma unroll
;                     for (int j = 0; j < 4; ++j) { const float a = fmaxf(v0[j], 0.f), b = fmaxf(v1[j], 0.f); v0[j] = a * a * 4.f; v1[j] = b * b * 4.f; }
;                     u32x2 w; w.x = pk4_fp8(v0[0], v0[1], v0[2], v0[3]); w.y = pk4_fp8(v1[0], v1[1], v1[2], v1[3]);
;                     *(u32x2*)(rowp + bj * (HALF / 32) * 512) = w;
	v_max_f32_e32 v23, 0, v23
	v_max_f32_e32 v25, 0, v27
	v_pk_mul_f32 v[14:15], v[14:15], v[14:15]
	v_pk_mul_f32 v[18:19], v[18:19], v[18:19]
	v_cvt_pk_fp8_f32 v8, v20, v21
	v_cvt_pk_fp8_f32 v9, v3, v12
	v_pk_mul_f32 v[22:23], v[22:23], v[22:23]
	v_pk_mul_f32 v[24:25], v[24:25], v[24:25]
	v_med3_f32 v14, v14, s44, v195
	v_med3_f32 v15, v15, s44, v195
	v_med3_f32 v18, v18, s44, v195
	v_med3_f32 v19, v19, s44, v195
	v_med3_f32 v22, v22, s44, v195
	v_med3_f32 v23, v23, s44, v195
	v_cvt_pk_fp8_f32 v6, v14, v15 op_sel:[0,0,1]
	v_cvt_pk_fp8_f32 v7, v18, v19 op_sel:[0,0,1]
	v_med3_f32 v3, v24, s44, v195
	v_med3_f32 v12, v25, s44, v195
	v_cvt_pk_fp8_f32 v8, v22, v23 op_sel:[0,0,1]
	v_cvt_pk_fp8_f32 v9, v3, v12 op_sel:[0,0,1]
	global_store_dwordx2 v[10:11], v[6:7], off
	global_store_dwordx2 v[10:11], v[8:9], off offset:2048
	v_add_u32_e32 v9, 0xa0, v2
	v_ashrrev_i32_e32 v10, 4, v9
	v_mov_b32_e32 v6, 0
	v_mov_b32_e32 v7, 0
	v_mov_b32_e32 v8, 0
	v_ashrrev_i32_e32 v11, 31, v10
	v_lshlrev_b64 v[10:11], 18, v[10:11]
	v_lshl_add_u64 v[10:11], s[24:25], 0, v[10:11]
	v_lshl_add_u64 v[10:11], v[10:11], 0, s[20:21]
	v_lshl_add_u64 v[10:11], v[10:11], 0, v[172:173]
	v_lshl_add_u64 v[10:11], v[10:11], 0, v[170:171]
	v_add_u32_e32 v2, 0xb0, v2
	v_ashrrev_i32_e32 v2, 4, v2
	v_fmamk_f32 v3, v240, 0x39800000, v194
	v_mul_f32_e32 v9, 0x4b800000, v3
	v_cmp_gt_f32_e32 vcc, s43, v3
	s_nop 1
	v_cndmask_b32_e32 v3, v3, v9, vcc
	v_rsq_f32_e32 v3, v3
	s_nop 0
	v_mul_f32_e32 v9, 0x45800000, v3
	v_cndmask_b32_e32 v3, v3, v9, vcc
	v_mul_f32_e32 v12, 0x3d000000, v3
	v_pk_mul_f32 v[16:17], v[62:63], v[12:13] op_sel_hi:[1,0]
	v_pk_mul_f32 v[20:21], v[58:59], v[12:13] op_sel_hi:[1,0]
	v_pk_mul_f32 v[14:15], v[64:65], v[12:13] op_sel_hi:[1,0]
	v_pk_mul_f32 v[18:19], v[60:61], v[12:13] op_sel_hi:[1,0]
	v_pk_mul_f32 v[22:23], v[56:57], v[12:13] op_sel_hi:[1,0]
	v_pk_mul_f32 v[24:25], v[54:55], v[12:13] op_sel_hi:[1,0]
	v_pk_mul_f32 v[26:27], v[52:53], v[12:13] op_sel_hi:[1,0]
	v_pk_mul_f32 v[12:13], v[50:51], v[12:13] op_sel_hi:[1,0]
	v_max_f32_e32 v3, 0, v16
	v_max_f32_e32 v9, 0, v20
	v_max_f32_e32 v16, 0, v17
	v_max_f32_e32 v17, 0, v21
	v_max_f32_e32 v20, 0, v24
	v_max_f32_e32 v12, 0, v12
	v_max_f32_e32 v21, 0, v25
	v_max_f32_e32 v13, 0, v13
	v_mul_f32_e32 v3, v3, v3
	v_mul_f32_e32 v9, v9, v9
	v_pk_mul_f32 v[16:17], v[16:17], v[16:17]
	v_pk_mul_f32 v[20:21], v[20:21], v[20:21]
	v_pk_mul_f32 v[12:13], v[12:13], v[12:13]
	v_med3_f32 v3, v3, s44, v195
	v_med3_f32 v16, v16, s44, v195
	v_med3_f32 v9, v9, s44, v195
	v_med3_f32 v17, v17, s44, v195
	v_max_f32_e32 v14, 0, v14
	v_max_f32_e32 v18, 0, v18
	v_max_f32_e32 v15, 0, v15
	v_max_f32_e32 v19, 0, v19
	v_med3_f32 v20, v20, s44, v195
	v_med3_f32 v21, v21, s44, v195
	v_med3_f32 v12, v12, s44, v195
	v_cvt_pk_fp8_f32 v6, v3, v16
	v_cvt_pk_fp8_f32 v7, v9, v17
	v_med3_f32 v3, v13, s44, v195
	v_mov_b32_e32 v9, 0
	v_max_f32_e32 v22, 0, v22
	v_max_f32_e32 v24, 0, v26
	v_max_f32_e32 v23, 0, v23
	v_max_f32_e32 v25, 0, v27
	v_pk_mul_f32 v[14:15], v[14:15], v[14:15]
	v_pk_mul_f32 v[18:19], v[18:19], v[18:19]
	v_cvt_pk_fp8_f32 v8, v20, v21
	v_cvt_pk_fp8_f32 v9, v12, v3
	v_pk_mul_f32 v[22:23], v[22:23], v[22:23]
	v_pk_mul_f32 v[24:25], v[24:25], v[24:25]
	v_med3_f32 v14, v14, s44, v195
	v_med3_f32 v15, v15, s44, v195
	v_med3_f32 v18, v18, s44, v195
	v_med3_f32 v19, v19, s44, v195
	v_med3_f32 v22, v22, s44, v195
	v_med3_f32 v23, v23, s44, v195
	v_cvt_pk_fp8_f32 v6, v14, v15 op_sel:[0,0,1]
	v_cvt_pk_fp8_f32 v7, v18, v19 op_sel:[0,0,1]
	v_med3_f32 v3, v24, s44, v195
	v_med3_f32 v12, v25, s44, v195
	v_cvt_pk_fp8_f32 v8, v22, v23 op_sel:[0,0,1]
	v_cvt_pk_fp8_f32 v9, v3, v12 op_sel:[0,0,1]
	global_store_dwordx2 v[10:11], v[6:7], off
	global_store_dwordx2 v[10:11], v[8:9], off offset:2048
	v_mov_b32_e32 v4, 0
	v_mov_b32_e32 v5, 0
	v_mov_b32_e32 v6, 0
	v_mov_b32_e32 v7, 0
	v_ashrrev_i32_e32 v3, 31, v2
	v_lshlrev_b64 v[2:3], 18, v[2:3]
	v_lshl_add_u64 v[2:3], s[24:25], 0, v[2:3]
	v_lshl_add_u64 v[2:3], v[2:3], 0, s[20:21]
	v_lshl_add_u64 v[2:3], v[2:3], 0, v[172:173]
	v_lshl_add_u64 v[2:3], v[2:3], 0, v[170:171]
	v_fmamk_f32 v8, v241, 0x39800000, v194
	v_mul_f32_e32 v9, 0x4b800000, v8
	v_cmp_gt_f32_e32 vcc, s43, v8
	s_nop 1
	v_cndmask_b32_e32 v8, v8, v9, vcc
	v_rsq_f32_e32 v8, v8
	s_nop 0
	v_mul_f32_e32 v9, 0x45800000, v8
	v_cndmask_b32_e32 v8, v8, v9, vcc
	v_mul_f32_e32 v8, 0x3d000000, v8
	v_pk_mul_f32 v[12:13], v[46:47], v[8:9] op_sel_hi:[1,0]
	v_pk_mul_f32 v[16:17], v[42:43], v[8:9] op_sel_hi:[1,0]
	v_pk_mul_f32 v[10:11], v[48:49], v[8:9] op_sel_hi:[1,0]
	v_pk_mul_f32 v[14:15], v[44:45], v[8:9] op_sel_hi:[1,0]
	v_pk_mul_f32 v[18:19], v[40:41], v[8:9] op_sel_hi:[1,0]
	v_pk_mul_f32 v[20:21], v[38:39], v[8:9] op_sel_hi:[1,0]
	v_pk_mul_f32 v[22:23], v[36:37], v[8:9] op_sel_hi:[1,0]
	v_pk_mul_f32 v[8:9], v[34:35], v[8:9] op_sel_hi:[1,0]
	v_max_f32_e32 v12, 0, v12
	v_max_f32_e32 v16, 0, v16
	v_max_f32_e32 v13, 0, v13
	v_max_f32_e32 v17, 0, v17
	v_max_f32_e32 v20, 0, v20
	v_max_f32_e32 v8, 0, v8
	v_max_f32_e32 v21, 0, v21
	v_max_f32_e32 v9, 0, v9
	v_pk_mul_f32 v[12:13], v[12:13], v[12:13]
	v_pk_mul_f32 v[16:17], v[16:17], v[16:17]
	v_pk_mul_f32 v[20:21], v[20:21], v[20:21]
	v_pk_mul_f32 v[8:9], v[8:9], v[8:9]
	v_med3_f32 v12, v12, s44, v195
	v_med3_f32 v13, v13, s44, v195
	v_med3_f32 v16, v16, s44, v195
	v_med3_f32 v17, v17, s44, v195
	v_max_f32_e32 v10, 0, v10
	v_max_f32_e32 v14, 0, v14
	v_max_f32_e32 v11, 0, v11
	v_max_f32_e32 v15, 0, v15
	v_med3_f32 v20, v20, s44, v195
	v_med3_f32 v21, v21, s44, v195
	v_med3_f32 v8, v8, s44, v195
	v_cvt_pk_fp8_f32 v4, v12, v13
	v_cvt_pk_fp8_f32 v5, v16, v17
	v_med3_f32 v9, v9, s44, v195
	v_max_f32_e32 v18, 0, v18
	v_max_f32_e32 v22, 0, v22
	v_max_f32_e32 v19, 0, v19
	v_max_f32_e32 v23, 0, v23
	v_pk_mul_f32 v[10:11], v[10:11], v[10:11]
	v_pk_mul_f32 v[14:15], v[14:15], v[14:15]
	v_cvt_pk_fp8_f32 v6, v20, v21
	v_cvt_pk_fp8_f32 v7, v8, v9
	v_pk_mul_f32 v[18:19], v[18:19], v[18:19]
	v_pk_mul_f32 v[22:23], v[22:23], v[22:23]
	v_med3_f32 v10, v10, s44, v195
	v_med3_f32 v11, v11, s44, v195
	v_med3_f32 v14, v14, s44, v195
	v_med3_f32 v15, v15, s44, v195
	v_med3_f32 v18, v18, s44, v195
	v_med3_f32 v19, v19, s44, v195
	v_cvt_pk_fp8_f32 v4, v10, v11 op_sel:[0,0,1]
	v_cvt_pk_fp8_f32 v5, v14, v15 op_sel:[0,0,1]
	v_med3_f32 v8, v22, s44, v195
	v_med3_f32 v9, v23, s44, v195
	v_cvt_pk_fp8_f32 v6, v18, v19 op_sel:[0,0,1]
	v_cvt_pk_fp8_f32 v7, v8, v9 op_sel:[0,0,1]
	s_andn2_b64 vcc, exec, s[0:1]
	s_mov_b64 s[0:1], -1
	global_store_dwordx2 v[2:3], v[4:5], off
	global_store_dwordx2 v[2:3], v[6:7], off offset:2048
	s_cbranch_vccnz .LBB0_2273
	s_andn2_b64 vcc, exec, s[4:5]
	s_cbranch_vccnz .LBB0_2272
	s_barrier
	s_branch .LBB0_2272
